# P0 rebalancing variant: GEMV workgroups 0-95 take a third conversion item (2.5 per wave on average)
# baseline (speedup 1.0000x reference)
.LBB0_41:
	s_or_b64 exec, exec, s[2:3]
	s_lshl_b32 s2, s80, 3
	s_add_i32 s16, s97, s2
	s_lshl_b32 s17, s62, 3
	s_movk_i32 s32, 0x2020
	s_cmpk_lg_i32 s62, 0x100
	s_cbranch_scc1 .Lp0_go
	s_cmpk_lt_u32 s80, 0xc0
	s_cbranch_scc0 .Lp0_tbl
	s_movk_i32 s17, 0x600
	s_movk_i32 s32, 0xc00
	s_cmpk_lt_u32 s80, 0x60
	s_cbranch_scc0 .Lp0_go
	s_movk_i32 s32, 0x1200
	s_branch .Lp0_go
.Lp0_tbl:
	s_addk_i32 s16, 0x900
	s_movk_i32 s17, 0x200
